# gates epilogue: the unit's seven remaining U-vector loads issued before (not after) the wait on the bias loads; on top of P4 rewrite, MoE LDS tables/bias prefetch, hand-written weight conversion
# speedup vs baseline: 1.0097x; 1.0044x over previous
.LBB0_1284:
	s_lshl_b32 s52, s48, 6
	v_mov_b32_e32 v96, v188
	v_mov_b32_e32 v98, v186
	s_and_b32 s52, s52, 0xffffff80
	s_lshl_b32 s48, s48, 12
	s_and_b32 s48, s48, 0x1000
	v_add_u32_e32 v116, s52, v96
	s_waitcnt lgkmcnt(0)
	s_add_u32 s52, s10, s48
	v_ashrrev_i32_e32 v117, 31, v116
	s_addc_u32 s53, s11, 0
	v_lshlrev_b64 v[118:119], 2, v[116:117]
	v_lshl_add_u64 v[136:137], s[52:53], 0, v[118:119]
	global_load_dwordx4 v[160:163], v[136:137], off offset:16
	global_load_dwordx4 v[164:167], v[136:137], off
	s_add_u32 s52, s12, s48
	s_addc_u32 s53, s13, 0
	v_lshl_add_u64 v[136:137], s[52:53], 0, v[118:119]
	global_load_dwordx4 v[192:195], v[136:137], off offset:16
	global_load_dwordx4 v[170:173], v[136:137], off
	v_add_u32_e32 v136, s77, v98
	v_ashrrev_i32_e32 v137, 31, v136
	v_lshlrev_b64 v[136:137], 11, v[136:137]
	s_add_u32 s52, s49, s48
	v_lshl_add_u64 v[136:137], s[8:9], 0, v[136:137]
	s_addc_u32 s53, s65, 0
	v_ashrrev_i32_e32 v99, 31, v98
	v_lshl_add_u64 v[116:117], v[116:117], 1, v[136:137]
	v_lshl_add_u64 v[118:119], s[52:53], 0, v[118:119]
	v_lshlrev_b64 v[98:99], 13, v[98:99]
	global_load_dwordx4 v[196:199], v[116:117], off
	global_load_dwordx4 v[200:203], v[118:119], off
	global_load_dwordx4 v[204:207], v[118:119], off offset:16
	s_mov_b32 s48, 0x8000
	v_ashrrev_i32_e32 v97, 31, v96
	v_lshl_add_u64 v[98:99], s[50:51], 0, v[98:99]
	v_lshl_add_u64 v[158:159], v[96:97], 1, v[98:99]
	v_add_co_u32_e32 v96, vcc, s48, v116
	s_mov_b32 s52, 0x10000
	s_nop 0
	v_addc_co_u32_e32 v97, vcc, 0, v117, vcc
	v_add_co_u32_e32 v98, vcc, s52, v116
	s_mov_b32 s53, 0x18000
	s_nop 0
	v_addc_co_u32_e32 v99, vcc, 0, v117, vcc
	v_add_co_u32_e32 v118, vcc, s53, v116
	s_mov_b32 s54, 0x48000
	s_nop 0
	v_addc_co_u32_e32 v119, vcc, 0, v117, vcc
	v_add_co_u32_e32 v136, vcc, s72, v116
	s_mov_b32 s55, 0x50000
	s_nop 0
	v_addc_co_u32_e32 v137, vcc, 0, v117, vcc
	v_add_co_u32_e32 v138, vcc, s54, v116
	s_mov_b32 s56, 0x58000
	s_nop 0
	v_addc_co_u32_e32 v139, vcc, 0, v117, vcc
	v_add_co_u32_e32 v168, vcc, s55, v116
	s_nop 1
	v_addc_co_u32_e32 v169, vcc, 0, v117, vcc
	v_add_co_u32_e32 v174, vcc, s56, v116
	s_nop 1
	v_addc_co_u32_e32 v175, vcc, 0, v117, vcc
	global_load_dwordx4 v[152:155], v[96:97], off
	global_load_dwordx4 v[148:151], v[98:99], off
	global_load_dwordx4 v[144:147], v[118:119], off
	global_load_dwordx4 v[140:143], v[136:137], off
	s_nop 0
	global_load_dwordx4 v[136:139], v[138:139], off
	s_nop 0
	global_load_dwordx4 v[116:119], v[168:169], off
	global_load_dwordx4 v[96:99], v[174:175], off
	s_waitcnt vmcnt(7)
	v_pk_mul_f32 v[162:163], v[162:163], s[20:21] op_sel_hi:[1,0]
	v_pk_mul_f32 v[176:177], v[170:171], s[20:21] op_sel_hi:[1,0]
	v_pk_mul_f32 v[174:175], v[166:167], s[20:21] op_sel_hi:[1,0]
	v_pk_mul_f32 v[168:169], v[160:161], s[20:21] op_sel_hi:[1,0]
	v_pk_fma_f32 v[134:135], v[134:135], s[22:23], v[174:175] op_sel_hi:[1,0,1] neg_lo:[1,0,0] neg_hi:[1,0,0]
	v_pk_fma_f32 v[128:129], v[128:129], s[22:23], v[176:177] op_sel_hi:[1,0,1] neg_lo:[1,0,0] neg_hi:[1,0,0]
	v_exp_f32_e32 v134, v134
	v_exp_f32_e32 v135, v135
	v_exp_f32_e32 v128, v128
	v_exp_f32_e32 v129, v129
	v_pk_fma_f32 v[124:125], v[124:125], s[22:23], v[168:169] op_sel_hi:[1,0,1] neg_lo:[1,0,0] neg_hi:[1,0,0]
	v_pk_add_f32 v[134:135], v[134:135], 1.0 op_sel_hi:[1,0]
	v_pk_mul_f32 v[180:181], v[164:165], s[20:21] op_sel_hi:[1,0]
	v_rcp_f32_e32 v134, v134
	v_rcp_f32_e32 v135, v135
	v_exp_f32_e32 v124, v124
	v_exp_f32_e32 v125, v125
	v_pk_fma_f32 v[126:127], v[126:127], s[22:23], v[162:163] op_sel_hi:[1,0,1] neg_lo:[1,0,0] neg_hi:[1,0,0]
	v_pk_fma_f32 v[208:209], v[132:133], s[22:23], v[180:181] op_sel_hi:[1,0,1] neg_lo:[1,0,0] neg_hi:[1,0,0]
	v_exp_f32_e32 v126, v126
	v_exp_f32_e32 v127, v127
	v_pk_mul_f32 v[170:171], v[172:173], s[20:21] op_sel_hi:[1,0]
	v_exp_f32_e32 v208, v208
	v_pk_mul_f32 v[172:173], v[202:203], s[22:23] op_sel_hi:[1,0]
	v_exp_f32_e32 v209, v209
	v_pk_add_f32 v[128:129], v[128:129], 1.0 op_sel_hi:[1,0]
	v_pk_fma_f32 v[130:131], v[130:131], s[22:23], v[170:171] op_sel_hi:[1,0,1] neg_lo:[1,0,0] neg_hi:[1,0,0]
	v_pk_mul_f32 v[134:135], v[172:173], v[134:135]
	v_rcp_f32_e32 v128, v128
	v_rcp_f32_e32 v129, v129
	v_exp_f32_e32 v130, v130
	v_exp_f32_e32 v131, v131
	v_exp_f32_e32 v134, v134
	v_exp_f32_e32 v135, v135
	v_pk_add_f32 v[124:125], v[124:125], 1.0 op_sel_hi:[1,0]
	v_pk_add_f32 v[126:127], v[126:127], 1.0 op_sel_hi:[1,0]
	v_rcp_f32_e32 v124, v124
	v_rcp_f32_e32 v125, v125
	v_pk_mul_f32 v[178:179], v[200:201], s[22:23] op_sel_hi:[1,0]
	v_pk_add_f32 v[200:201], v[208:209], 1.0 op_sel_hi:[1,0]
	v_rcp_f32_e32 v126, v126
	v_rcp_f32_e32 v127, v127
	v_pk_mul_f32 v[164:165], v[192:193], s[20:21] op_sel_hi:[1,0]
	v_lshlrev_b32_e32 v192, 16, v196
	v_and_b32_e32 v193, 0xffff0000, v196
	v_rcp_f32_e32 v200, v200
	v_rcp_f32_e32 v201, v201
	v_pk_mul_f32 v[166:167], v[204:205], s[22:23] op_sel_hi:[1,0]
	v_pk_mul_f32 v[128:129], v[128:129], v[192:193]
	v_pk_add_f32 v[130:131], v[130:131], 1.0 op_sel_hi:[1,0]
	v_pk_add_f32 v[192:193], v[134:135], 1.0 op_sel_hi:[1,0] neg_lo:[1,0] neg_hi:[1,0]
	v_pk_add_f32 v[134:135], v[134:135], 1.0 op_sel_hi:[1,0]
	v_pk_mul_f32 v[160:161], v[194:195], s[20:21] op_sel_hi:[1,0]
	v_pk_mul_f32 v[132:133], v[206:207], s[22:23] op_sel_hi:[1,0]
	v_rcp_f32_e32 v130, v130
	v_rcp_f32_e32 v131, v131
	v_pk_mul_f32 v[134:135], v[192:193], v[134:135]
	v_pk_fma_f32 v[120:121], v[120:121], s[22:23], v[164:165] op_sel_hi:[1,0,1] neg_lo:[1,0,0] neg_hi:[1,0,0]
	v_pk_mul_f32 v[124:125], v[166:167], v[124:125]
	v_sqrt_f32_e32 v134, v134
	v_sqrt_f32_e32 v135, v135
	v_exp_f32_e32 v120, v120
	v_exp_f32_e32 v121, v121
	v_exp_f32_e32 v124, v124
	v_exp_f32_e32 v125, v125
	v_pk_fma_f32 v[122:123], v[122:123], s[22:23], v[160:161] op_sel_hi:[1,0,1] neg_lo:[1,0,0] neg_hi:[1,0,0]
	v_pk_mul_f32 v[126:127], v[132:133], v[126:127]
	v_pk_mul_f32 v[200:201], v[178:179], v[200:201]
	v_exp_f32_e32 v122, v122
	v_exp_f32_e32 v123, v123
	v_exp_f32_e32 v126, v126
	v_exp_f32_e32 v127, v127
	v_lshlrev_b32_e32 v194, 16, v197
	v_and_b32_e32 v195, 0xffff0000, v197
	v_exp_f32_e32 v200, v200
	v_exp_f32_e32 v201, v201
	v_pk_mul_f32 v[130:131], v[130:131], v[194:195]
	v_pk_add_f32 v[120:121], v[120:121], 1.0 op_sel_hi:[1,0]
	v_pk_mul_f32 v[130:131], v[130:131], v[134:135]
	v_pk_add_f32 v[134:135], v[124:125], 1.0 op_sel_hi:[1,0] neg_lo:[1,0] neg_hi:[1,0]
	v_pk_add_f32 v[124:125], v[124:125], 1.0 op_sel_hi:[1,0]
	v_rcp_f32_e32 v120, v120
	v_rcp_f32_e32 v121, v121
	v_pk_mul_f32 v[124:125], v[134:135], v[124:125]
	v_pk_add_f32 v[122:123], v[122:123], 1.0 op_sel_hi:[1,0]
	v_pk_add_f32 v[194:195], v[126:127], 1.0 op_sel_hi:[1,0] neg_lo:[1,0] neg_hi:[1,0]
	v_pk_add_f32 v[126:127], v[126:127], 1.0 op_sel_hi:[1,0]
	v_pk_add_f32 v[202:203], v[200:201], 1.0 op_sel_hi:[1,0] neg_lo:[1,0] neg_hi:[1,0]
	v_pk_add_f32 v[200:201], v[200:201], 1.0 op_sel_hi:[1,0]
	v_sqrt_f32_e32 v124, v124
	v_sqrt_f32_e32 v125, v125
	v_rcp_f32_e32 v122, v122
	v_rcp_f32_e32 v123, v123
	v_pk_mul_f32 v[126:127], v[194:195], v[126:127]
	v_pk_mul_f32 v[200:201], v[202:203], v[200:201]
	v_sqrt_f32_e32 v126, v126
	v_sqrt_f32_e32 v127, v127
	v_lshlrev_b32_e32 v196, 16, v198
	v_and_b32_e32 v197, 0xffff0000, v198
	v_sqrt_f32_e32 v200, v200
	v_sqrt_f32_e32 v201, v201
	v_lshlrev_b32_e32 v198, 16, v199
	v_and_b32_e32 v199, 0xffff0000, v199
	v_pk_mul_f32 v[120:121], v[120:121], v[196:197]
	v_pk_mul_f32 v[128:129], v[128:129], v[200:201]
	v_pk_mul_f32 v[124:125], v[120:121], v[124:125]
	v_pk_mul_f32 v[120:121], v[122:123], v[198:199]
	v_cvt_pk_bf16_f32 v122, v134, v135
	v_cvt_pk_bf16_f32 v123, v194, v195
	s_nop 0
	v_pk_mul_f32 v[126:127], v[120:121], v[126:127]
	v_cvt_pk_bf16_f32 v120, v202, v203
	v_cvt_pk_bf16_f32 v121, v192, v193
	global_store_dwordx4 v[158:159], v[120:123], off
	s_nop 1
	v_cvt_pk_bf16_f32 v120, v128, v129
	v_cvt_pk_bf16_f32 v121, v130, v131
	v_cvt_pk_bf16_f32 v122, v124, v125
	v_cvt_pk_bf16_f32 v123, v126, v127
	global_store_dwordx4 v[158:159], v[120:123], off offset:256
	v_pk_fma_f32 v[112:113], v[112:113], s[22:23], v[180:181] op_sel_hi:[1,0,1] neg_lo:[1,0,0] neg_hi:[1,0,0]
	v_pk_fma_f32 v[114:115], v[114:115], s[22:23], v[174:175] op_sel_hi:[1,0,1] neg_lo:[1,0,0] neg_hi:[1,0,0]
	v_exp_f32_e32 v112, v112
	v_exp_f32_e32 v113, v113
	v_exp_f32_e32 v114, v114
	v_exp_f32_e32 v115, v115
	v_pk_fma_f32 v[108:109], v[108:109], s[22:23], v[176:177] op_sel_hi:[1,0,1] neg_lo:[1,0,0] neg_hi:[1,0,0]
	v_pk_add_f32 v[112:113], v[112:113], 1.0 op_sel_hi:[1,0]
	v_pk_fma_f32 v[104:105], v[104:105], s[22:23], v[168:169] op_sel_hi:[1,0,1] neg_lo:[1,0,0] neg_hi:[1,0,0]
	v_rcp_f32_e32 v112, v112
	v_rcp_f32_e32 v113, v113
	v_pk_add_f32 v[114:115], v[114:115], 1.0 op_sel_hi:[1,0]
	v_exp_f32_e32 v108, v108
	v_exp_f32_e32 v109, v109
	v_rcp_f32_e32 v114, v114
	v_rcp_f32_e32 v115, v115
	v_exp_f32_e32 v104, v104
	v_exp_f32_e32 v105, v105
	v_pk_fma_f32 v[106:107], v[106:107], s[22:23], v[162:163] op_sel_hi:[1,0,1] neg_lo:[1,0,0] neg_hi:[1,0,0]
	v_pk_mul_f32 v[112:113], v[178:179], v[112:113]
	v_exp_f32_e32 v106, v106
	v_exp_f32_e32 v107, v107
	v_exp_f32_e32 v112, v112
	v_exp_f32_e32 v113, v113
	v_pk_add_f32 v[108:109], v[108:109], 1.0 op_sel_hi:[1,0]
	v_pk_fma_f32 v[110:111], v[110:111], s[22:23], v[170:171] op_sel_hi:[1,0,1] neg_lo:[1,0,0] neg_hi:[1,0,0]
	v_pk_mul_f32 v[114:115], v[172:173], v[114:115]
	v_pk_add_f32 v[104:105], v[104:105], 1.0 op_sel_hi:[1,0]
	v_rcp_f32_e32 v108, v108
	v_rcp_f32_e32 v109, v109
	v_exp_f32_e32 v110, v110
	v_exp_f32_e32 v111, v111
	v_exp_f32_e32 v114, v114
	v_exp_f32_e32 v115, v115
	v_rcp_f32_e32 v104, v104
	v_rcp_f32_e32 v105, v105
	v_pk_add_f32 v[106:107], v[106:107], 1.0 op_sel_hi:[1,0]
	s_waitcnt vmcnt(8)
	v_lshlrev_b32_e32 v120, 16, v152
	v_rcp_f32_e32 v106, v106
	v_rcp_f32_e32 v107, v107
	v_and_b32_e32 v121, 0xffff0000, v152
	v_pk_add_f32 v[128:129], v[112:113], 1.0 op_sel_hi:[1,0] neg_lo:[1,0] neg_hi:[1,0]
	v_pk_add_f32 v[112:113], v[112:113], 1.0 op_sel_hi:[1,0]
	v_pk_mul_f32 v[108:109], v[108:109], v[120:121]
	v_pk_mul_f32 v[112:113], v[128:129], v[112:113]
	v_pk_add_f32 v[110:111], v[110:111], 1.0 op_sel_hi:[1,0]
	v_pk_add_f32 v[120:121], v[114:115], 1.0 op_sel_hi:[1,0] neg_lo:[1,0] neg_hi:[1,0]
	v_pk_add_f32 v[114:115], v[114:115], 1.0 op_sel_hi:[1,0]
	v_pk_fma_f32 v[100:101], v[100:101], s[22:23], v[164:165] op_sel_hi:[1,0,1] neg_lo:[1,0,0] neg_hi:[1,0,0]
	v_pk_mul_f32 v[104:105], v[166:167], v[104:105]
	v_sqrt_f32_e32 v112, v112
	v_sqrt_f32_e32 v113, v113
	v_rcp_f32_e32 v110, v110
	v_rcp_f32_e32 v111, v111
	v_pk_mul_f32 v[114:115], v[120:121], v[114:115]
	v_exp_f32_e32 v100, v100
	v_exp_f32_e32 v101, v101
	v_exp_f32_e32 v104, v104
	v_exp_f32_e32 v105, v105
	v_pk_fma_f32 v[102:103], v[102:103], s[22:23], v[160:161] op_sel_hi:[1,0,1] neg_lo:[1,0,0] neg_hi:[1,0,0]
	v_pk_mul_f32 v[106:107], v[132:133], v[106:107]
	v_sqrt_f32_e32 v114, v114
	v_sqrt_f32_e32 v115, v115
	v_exp_f32_e32 v102, v102
	v_exp_f32_e32 v103, v103
	v_exp_f32_e32 v106, v106
	v_exp_f32_e32 v107, v107
	v_lshlrev_b32_e32 v122, 16, v153
	v_and_b32_e32 v123, 0xffff0000, v153
	v_pk_mul_f32 v[108:109], v[108:109], v[112:113]
	v_pk_mul_f32 v[110:111], v[110:111], v[122:123]
	v_pk_add_f32 v[100:101], v[100:101], 1.0 op_sel_hi:[1,0]
	v_pk_add_f32 v[112:113], v[104:105], 1.0 op_sel_hi:[1,0] neg_lo:[1,0] neg_hi:[1,0]
	v_pk_add_f32 v[104:105], v[104:105], 1.0 op_sel_hi:[1,0]
	v_pk_mul_f32 v[110:111], v[110:111], v[114:115]
	v_rcp_f32_e32 v100, v100
	v_rcp_f32_e32 v101, v101
	v_pk_mul_f32 v[104:105], v[112:113], v[104:105]
	v_pk_add_f32 v[102:103], v[102:103], 1.0 op_sel_hi:[1,0]
	v_pk_add_f32 v[114:115], v[106:107], 1.0 op_sel_hi:[1,0] neg_lo:[1,0] neg_hi:[1,0]
	v_pk_add_f32 v[106:107], v[106:107], 1.0 op_sel_hi:[1,0]
	v_sqrt_f32_e32 v104, v104
	v_sqrt_f32_e32 v105, v105
	v_rcp_f32_e32 v102, v102
	v_rcp_f32_e32 v103, v103
	v_pk_mul_f32 v[106:107], v[114:115], v[106:107]
	v_lshlrev_b32_e32 v124, 16, v154
	v_sqrt_f32_e32 v106, v106
	v_sqrt_f32_e32 v107, v107
	v_and_b32_e32 v125, 0xffff0000, v154
	v_lshlrev_b32_e32 v126, 16, v155
	v_and_b32_e32 v127, 0xffff0000, v155
	v_pk_mul_f32 v[100:101], v[100:101], v[124:125]
	s_mov_b32 s48, 0x20000
	v_pk_mul_f32 v[104:105], v[100:101], v[104:105]
	v_pk_mul_f32 v[100:101], v[102:103], v[126:127]
	v_cvt_pk_bf16_f32 v102, v112, v113
	v_add_co_u32_e32 v112, vcc, s48, v158
	v_pk_mul_f32 v[106:107], v[100:101], v[106:107]
	v_cvt_pk_bf16_f32 v100, v128, v129
	v_cvt_pk_bf16_f32 v101, v120, v121
	v_cvt_pk_bf16_f32 v103, v114, v115
	s_nop 0
	v_addc_co_u32_e32 v113, vcc, 0, v159, vcc
	global_store_dwordx4 v[112:113], v[100:103], off
	s_nop 1
	v_cvt_pk_bf16_f32 v100, v108, v109
	v_cvt_pk_bf16_f32 v101, v110, v111
	v_cvt_pk_bf16_f32 v102, v104, v105
	v_cvt_pk_bf16_f32 v103, v106, v107
	global_store_dwordx4 v[112:113], v[100:103], off offset:256
	v_pk_fma_f32 v[92:93], v[92:93], s[22:23], v[180:181] op_sel_hi:[1,0,1] neg_lo:[1,0,0] neg_hi:[1,0,0]
	v_pk_fma_f32 v[94:95], v[94:95], s[22:23], v[174:175] op_sel_hi:[1,0,1] neg_lo:[1,0,0] neg_hi:[1,0,0]
	v_exp_f32_e32 v92, v92
	v_exp_f32_e32 v93, v93
	v_exp_f32_e32 v94, v94
	v_exp_f32_e32 v95, v95
	v_pk_fma_f32 v[88:89], v[88:89], s[22:23], v[176:177] op_sel_hi:[1,0,1] neg_lo:[1,0,0] neg_hi:[1,0,0]
	v_pk_add_f32 v[92:93], v[92:93], 1.0 op_sel_hi:[1,0]
	v_pk_fma_f32 v[84:85], v[84:85], s[22:23], v[168:169] op_sel_hi:[1,0,1] neg_lo:[1,0,0] neg_hi:[1,0,0]
	v_rcp_f32_e32 v92, v92
	v_rcp_f32_e32 v93, v93
	v_pk_add_f32 v[94:95], v[94:95], 1.0 op_sel_hi:[1,0]
	v_exp_f32_e32 v88, v88
	v_exp_f32_e32 v89, v89
	v_rcp_f32_e32 v94, v94
	v_rcp_f32_e32 v95, v95
	v_exp_f32_e32 v84, v84
	v_exp_f32_e32 v85, v85
	v_pk_fma_f32 v[86:87], v[86:87], s[22:23], v[162:163] op_sel_hi:[1,0,1] neg_lo:[1,0,0] neg_hi:[1,0,0]
	v_pk_mul_f32 v[92:93], v[178:179], v[92:93]
	v_exp_f32_e32 v86, v86
	v_exp_f32_e32 v87, v87
	v_exp_f32_e32 v92, v92
	v_exp_f32_e32 v93, v93
	v_pk_add_f32 v[88:89], v[88:89], 1.0 op_sel_hi:[1,0]
	v_pk_fma_f32 v[90:91], v[90:91], s[22:23], v[170:171] op_sel_hi:[1,0,1] neg_lo:[1,0,0] neg_hi:[1,0,0]
	v_pk_mul_f32 v[94:95], v[172:173], v[94:95]
	v_pk_add_f32 v[84:85], v[84:85], 1.0 op_sel_hi:[1,0]
	v_rcp_f32_e32 v88, v88
	v_rcp_f32_e32 v89, v89
	v_exp_f32_e32 v90, v90
	v_exp_f32_e32 v91, v91
	v_exp_f32_e32 v94, v94
	v_exp_f32_e32 v95, v95
	v_rcp_f32_e32 v84, v84
	v_rcp_f32_e32 v85, v85
	v_pk_add_f32 v[86:87], v[86:87], 1.0 op_sel_hi:[1,0]
	s_waitcnt vmcnt(9)
	v_lshlrev_b32_e32 v100, 16, v148
	v_rcp_f32_e32 v86, v86
	v_rcp_f32_e32 v87, v87
	v_and_b32_e32 v101, 0xffff0000, v148
	v_pk_add_f32 v[108:109], v[92:93], 1.0 op_sel_hi:[1,0] neg_lo:[1,0] neg_hi:[1,0]
	v_pk_add_f32 v[92:93], v[92:93], 1.0 op_sel_hi:[1,0]
	v_pk_mul_f32 v[88:89], v[88:89], v[100:101]
	v_pk_mul_f32 v[92:93], v[108:109], v[92:93]
	v_pk_add_f32 v[90:91], v[90:91], 1.0 op_sel_hi:[1,0]
	v_pk_add_f32 v[100:101], v[94:95], 1.0 op_sel_hi:[1,0] neg_lo:[1,0] neg_hi:[1,0]
	v_pk_add_f32 v[94:95], v[94:95], 1.0 op_sel_hi:[1,0]
	v_pk_fma_f32 v[80:81], v[80:81], s[22:23], v[164:165] op_sel_hi:[1,0,1] neg_lo:[1,0,0] neg_hi:[1,0,0]
	v_pk_mul_f32 v[84:85], v[166:167], v[84:85]
	v_sqrt_f32_e32 v92, v92
	v_sqrt_f32_e32 v93, v93
	v_rcp_f32_e32 v90, v90
	v_rcp_f32_e32 v91, v91
	v_pk_mul_f32 v[94:95], v[100:101], v[94:95]
	v_exp_f32_e32 v80, v80
	v_exp_f32_e32 v81, v81
	v_exp_f32_e32 v84, v84
	v_exp_f32_e32 v85, v85
	v_pk_fma_f32 v[82:83], v[82:83], s[22:23], v[160:161] op_sel_hi:[1,0,1] neg_lo:[1,0,0] neg_hi:[1,0,0]
	v_pk_mul_f32 v[86:87], v[132:133], v[86:87]
	v_sqrt_f32_e32 v94, v94
	v_sqrt_f32_e32 v95, v95
	v_exp_f32_e32 v82, v82
	v_exp_f32_e32 v83, v83
	v_exp_f32_e32 v86, v86
	v_exp_f32_e32 v87, v87
	v_lshlrev_b32_e32 v102, 16, v149
	v_and_b32_e32 v103, 0xffff0000, v149
	v_pk_mul_f32 v[88:89], v[88:89], v[92:93]
	v_pk_mul_f32 v[90:91], v[90:91], v[102:103]
	v_pk_add_f32 v[80:81], v[80:81], 1.0 op_sel_hi:[1,0]
	v_pk_add_f32 v[92:93], v[84:85], 1.0 op_sel_hi:[1,0] neg_lo:[1,0] neg_hi:[1,0]
	v_pk_add_f32 v[84:85], v[84:85], 1.0 op_sel_hi:[1,0]
	v_pk_mul_f32 v[90:91], v[90:91], v[94:95]
	v_rcp_f32_e32 v80, v80
	v_rcp_f32_e32 v81, v81
	v_pk_mul_f32 v[84:85], v[92:93], v[84:85]
	v_pk_add_f32 v[82:83], v[82:83], 1.0 op_sel_hi:[1,0]
	v_pk_add_f32 v[94:95], v[86:87], 1.0 op_sel_hi:[1,0] neg_lo:[1,0] neg_hi:[1,0]
	v_pk_add_f32 v[86:87], v[86:87], 1.0 op_sel_hi:[1,0]
	v_sqrt_f32_e32 v84, v84
	v_sqrt_f32_e32 v85, v85
	v_rcp_f32_e32 v82, v82
	v_rcp_f32_e32 v83, v83
	v_pk_mul_f32 v[86:87], v[94:95], v[86:87]
	v_lshlrev_b32_e32 v104, 16, v150
	v_sqrt_f32_e32 v86, v86
	v_sqrt_f32_e32 v87, v87
	v_and_b32_e32 v105, 0xffff0000, v150
	v_lshlrev_b32_e32 v106, 16, v151
	v_and_b32_e32 v107, 0xffff0000, v151
	v_pk_mul_f32 v[80:81], v[80:81], v[104:105]
	s_nop 0
	v_pk_mul_f32 v[84:85], v[80:81], v[84:85]
	v_pk_mul_f32 v[80:81], v[82:83], v[106:107]
	v_cvt_pk_bf16_f32 v82, v92, v93
	v_add_co_u32_e32 v92, vcc, s72, v158
	v_pk_mul_f32 v[86:87], v[80:81], v[86:87]
	v_cvt_pk_bf16_f32 v80, v108, v109
	v_cvt_pk_bf16_f32 v81, v100, v101
	v_cvt_pk_bf16_f32 v83, v94, v95
	s_nop 0
	v_addc_co_u32_e32 v93, vcc, 0, v159, vcc
	global_store_dwordx4 v[92:93], v[80:83], off
	s_nop 1
	v_cvt_pk_bf16_f32 v80, v88, v89
	v_cvt_pk_bf16_f32 v81, v90, v91
	v_cvt_pk_bf16_f32 v82, v84, v85
	v_cvt_pk_bf16_f32 v83, v86, v87
	global_store_dwordx4 v[92:93], v[80:83], off offset:256
	v_pk_fma_f32 v[76:77], v[76:77], s[22:23], v[180:181] op_sel_hi:[1,0,1] neg_lo:[1,0,0] neg_hi:[1,0,0]
	v_pk_fma_f32 v[78:79], v[78:79], s[22:23], v[174:175] op_sel_hi:[1,0,1] neg_lo:[1,0,0] neg_hi:[1,0,0]
	v_exp_f32_e32 v76, v76
	v_exp_f32_e32 v77, v77
	v_exp_f32_e32 v78, v78
	v_exp_f32_e32 v79, v79
	v_pk_fma_f32 v[72:73], v[72:73], s[22:23], v[176:177] op_sel_hi:[1,0,1] neg_lo:[1,0,0] neg_hi:[1,0,0]
	v_pk_add_f32 v[76:77], v[76:77], 1.0 op_sel_hi:[1,0]
	v_pk_fma_f32 v[68:69], v[68:69], s[22:23], v[168:169] op_sel_hi:[1,0,1] neg_lo:[1,0,0] neg_hi:[1,0,0]
	v_rcp_f32_e32 v76, v76
	v_rcp_f32_e32 v77, v77
	v_pk_add_f32 v[78:79], v[78:79], 1.0 op_sel_hi:[1,0]
	v_exp_f32_e32 v72, v72
	v_exp_f32_e32 v73, v73
	v_rcp_f32_e32 v78, v78
	v_rcp_f32_e32 v79, v79
	v_exp_f32_e32 v68, v68
	v_exp_f32_e32 v69, v69
	v_pk_fma_f32 v[70:71], v[70:71], s[22:23], v[162:163] op_sel_hi:[1,0,1] neg_lo:[1,0,0] neg_hi:[1,0,0]
	v_pk_mul_f32 v[76:77], v[178:179], v[76:77]
	v_exp_f32_e32 v70, v70
	v_exp_f32_e32 v71, v71
	v_exp_f32_e32 v76, v76
	v_exp_f32_e32 v77, v77
	v_pk_add_f32 v[72:73], v[72:73], 1.0 op_sel_hi:[1,0]
	v_pk_fma_f32 v[74:75], v[74:75], s[22:23], v[170:171] op_sel_hi:[1,0,1] neg_lo:[1,0,0] neg_hi:[1,0,0]
	v_pk_mul_f32 v[78:79], v[172:173], v[78:79]
	v_pk_add_f32 v[68:69], v[68:69], 1.0 op_sel_hi:[1,0]
	v_rcp_f32_e32 v72, v72
	v_rcp_f32_e32 v73, v73
	v_exp_f32_e32 v74, v74
	v_exp_f32_e32 v75, v75
	v_exp_f32_e32 v78, v78
	v_exp_f32_e32 v79, v79
	v_rcp_f32_e32 v68, v68
	v_rcp_f32_e32 v69, v69
	v_pk_add_f32 v[70:71], v[70:71], 1.0 op_sel_hi:[1,0]
	s_waitcnt vmcnt(10)
	v_lshlrev_b32_e32 v80, 16, v144
	v_rcp_f32_e32 v70, v70
	v_rcp_f32_e32 v71, v71
	v_and_b32_e32 v81, 0xffff0000, v144
	v_pk_add_f32 v[88:89], v[76:77], 1.0 op_sel_hi:[1,0] neg_lo:[1,0] neg_hi:[1,0]
	v_pk_add_f32 v[76:77], v[76:77], 1.0 op_sel_hi:[1,0]
	v_pk_mul_f32 v[72:73], v[72:73], v[80:81]
	v_pk_mul_f32 v[76:77], v[88:89], v[76:77]
	v_pk_add_f32 v[74:75], v[74:75], 1.0 op_sel_hi:[1,0]
	v_pk_add_f32 v[80:81], v[78:79], 1.0 op_sel_hi:[1,0] neg_lo:[1,0] neg_hi:[1,0]
	v_pk_add_f32 v[78:79], v[78:79], 1.0 op_sel_hi:[1,0]
	v_pk_fma_f32 v[64:65], v[64:65], s[22:23], v[164:165] op_sel_hi:[1,0,1] neg_lo:[1,0,0] neg_hi:[1,0,0]
	v_pk_mul_f32 v[68:69], v[166:167], v[68:69]
	v_sqrt_f32_e32 v76, v76
	v_sqrt_f32_e32 v77, v77
	v_rcp_f32_e32 v74, v74
	v_rcp_f32_e32 v75, v75
	v_pk_mul_f32 v[78:79], v[80:81], v[78:79]
	v_exp_f32_e32 v64, v64
	v_exp_f32_e32 v65, v65
	v_exp_f32_e32 v68, v68
	v_exp_f32_e32 v69, v69
	v_pk_fma_f32 v[66:67], v[66:67], s[22:23], v[160:161] op_sel_hi:[1,0,1] neg_lo:[1,0,0] neg_hi:[1,0,0]
	v_pk_mul_f32 v[70:71], v[132:133], v[70:71]
	v_sqrt_f32_e32 v78, v78
	v_sqrt_f32_e32 v79, v79
	v_exp_f32_e32 v66, v66
	v_exp_f32_e32 v67, v67
	v_exp_f32_e32 v70, v70
	v_exp_f32_e32 v71, v71
	v_lshlrev_b32_e32 v82, 16, v145
	v_and_b32_e32 v83, 0xffff0000, v145
	v_pk_mul_f32 v[72:73], v[72:73], v[76:77]
	v_pk_mul_f32 v[74:75], v[74:75], v[82:83]
	v_pk_add_f32 v[64:65], v[64:65], 1.0 op_sel_hi:[1,0]
	v_pk_add_f32 v[76:77], v[68:69], 1.0 op_sel_hi:[1,0] neg_lo:[1,0] neg_hi:[1,0]
	v_pk_add_f32 v[68:69], v[68:69], 1.0 op_sel_hi:[1,0]
	v_pk_mul_f32 v[74:75], v[74:75], v[78:79]
	v_rcp_f32_e32 v64, v64
	v_rcp_f32_e32 v65, v65
	v_pk_mul_f32 v[68:69], v[76:77], v[68:69]
	v_pk_add_f32 v[66:67], v[66:67], 1.0 op_sel_hi:[1,0]
	v_pk_add_f32 v[78:79], v[70:71], 1.0 op_sel_hi:[1,0] neg_lo:[1,0] neg_hi:[1,0]
	v_pk_add_f32 v[70:71], v[70:71], 1.0 op_sel_hi:[1,0]
	v_sqrt_f32_e32 v68, v68
	v_sqrt_f32_e32 v69, v69
	v_rcp_f32_e32 v66, v66
	v_rcp_f32_e32 v67, v67
	v_pk_mul_f32 v[70:71], v[78:79], v[70:71]
	v_lshlrev_b32_e32 v84, 16, v146
	v_sqrt_f32_e32 v70, v70
	v_sqrt_f32_e32 v71, v71
	v_and_b32_e32 v85, 0xffff0000, v146
	v_lshlrev_b32_e32 v86, 16, v147
	v_and_b32_e32 v87, 0xffff0000, v147
	v_pk_mul_f32 v[64:65], v[64:65], v[84:85]
	s_nop 0
	v_pk_mul_f32 v[68:69], v[64:65], v[68:69]
	v_pk_mul_f32 v[64:65], v[66:67], v[86:87]
	v_cvt_pk_bf16_f32 v66, v76, v77
	v_add_co_u32_e32 v76, vcc, s73, v158
	v_pk_mul_f32 v[70:71], v[64:65], v[70:71]
	v_cvt_pk_bf16_f32 v64, v88, v89
	v_cvt_pk_bf16_f32 v65, v80, v81
	v_cvt_pk_bf16_f32 v67, v78, v79
	s_nop 0
	v_addc_co_u32_e32 v77, vcc, 0, v159, vcc
	global_store_dwordx4 v[76:77], v[64:67], off
	s_nop 1
	v_cvt_pk_bf16_f32 v64, v72, v73
	v_cvt_pk_bf16_f32 v65, v74, v75
	v_cvt_pk_bf16_f32 v66, v68, v69
	v_cvt_pk_bf16_f32 v67, v70, v71
	global_store_dwordx4 v[76:77], v[64:67], off offset:256
	v_pk_fma_f32 v[60:61], v[60:61], s[22:23], v[180:181] op_sel_hi:[1,0,1] neg_lo:[1,0,0] neg_hi:[1,0,0]
	v_pk_fma_f32 v[62:63], v[62:63], s[22:23], v[174:175] op_sel_hi:[1,0,1] neg_lo:[1,0,0] neg_hi:[1,0,0]
	v_exp_f32_e32 v60, v60
	v_exp_f32_e32 v61, v61
	v_exp_f32_e32 v62, v62
	v_exp_f32_e32 v63, v63
	v_pk_fma_f32 v[56:57], v[56:57], s[22:23], v[176:177] op_sel_hi:[1,0,1] neg_lo:[1,0,0] neg_hi:[1,0,0]
	v_pk_add_f32 v[60:61], v[60:61], 1.0 op_sel_hi:[1,0]
	v_pk_fma_f32 v[52:53], v[52:53], s[22:23], v[168:169] op_sel_hi:[1,0,1] neg_lo:[1,0,0] neg_hi:[1,0,0]
	v_rcp_f32_e32 v60, v60
	v_rcp_f32_e32 v61, v61
	v_pk_add_f32 v[62:63], v[62:63], 1.0 op_sel_hi:[1,0]
	v_exp_f32_e32 v56, v56
	v_exp_f32_e32 v57, v57
	v_rcp_f32_e32 v62, v62
	v_rcp_f32_e32 v63, v63
	v_exp_f32_e32 v52, v52
	v_exp_f32_e32 v53, v53
	v_pk_fma_f32 v[54:55], v[54:55], s[22:23], v[162:163] op_sel_hi:[1,0,1] neg_lo:[1,0,0] neg_hi:[1,0,0]
	v_pk_mul_f32 v[60:61], v[178:179], v[60:61]
	v_exp_f32_e32 v54, v54
	v_exp_f32_e32 v55, v55
	v_exp_f32_e32 v60, v60
	v_exp_f32_e32 v61, v61
	v_pk_add_f32 v[56:57], v[56:57], 1.0 op_sel_hi:[1,0]
	v_pk_fma_f32 v[58:59], v[58:59], s[22:23], v[170:171] op_sel_hi:[1,0,1] neg_lo:[1,0,0] neg_hi:[1,0,0]
	v_pk_mul_f32 v[62:63], v[172:173], v[62:63]
	v_pk_add_f32 v[52:53], v[52:53], 1.0 op_sel_hi:[1,0]
	v_rcp_f32_e32 v56, v56
	v_rcp_f32_e32 v57, v57
	v_exp_f32_e32 v58, v58
	v_exp_f32_e32 v59, v59
	v_exp_f32_e32 v62, v62
	v_exp_f32_e32 v63, v63
	v_rcp_f32_e32 v52, v52
	v_rcp_f32_e32 v53, v53
	v_pk_add_f32 v[54:55], v[54:55], 1.0 op_sel_hi:[1,0]
	s_waitcnt vmcnt(11)
	v_lshlrev_b32_e32 v64, 16, v140
	v_rcp_f32_e32 v54, v54
	v_rcp_f32_e32 v55, v55
	v_and_b32_e32 v65, 0xffff0000, v140
	v_pk_add_f32 v[72:73], v[60:61], 1.0 op_sel_hi:[1,0] neg_lo:[1,0] neg_hi:[1,0]
	v_pk_add_f32 v[60:61], v[60:61], 1.0 op_sel_hi:[1,0]
	v_pk_mul_f32 v[56:57], v[56:57], v[64:65]
	v_pk_mul_f32 v[60:61], v[72:73], v[60:61]
	v_pk_add_f32 v[58:59], v[58:59], 1.0 op_sel_hi:[1,0]
	v_pk_add_f32 v[64:65], v[62:63], 1.0 op_sel_hi:[1,0] neg_lo:[1,0] neg_hi:[1,0]
	v_pk_add_f32 v[62:63], v[62:63], 1.0 op_sel_hi:[1,0]
	v_pk_fma_f32 v[48:49], v[48:49], s[22:23], v[164:165] op_sel_hi:[1,0,1] neg_lo:[1,0,0] neg_hi:[1,0,0]
	v_pk_mul_f32 v[52:53], v[166:167], v[52:53]
	v_sqrt_f32_e32 v60, v60
	v_sqrt_f32_e32 v61, v61
	v_rcp_f32_e32 v58, v58
	v_rcp_f32_e32 v59, v59
	v_pk_mul_f32 v[62:63], v[64:65], v[62:63]
	v_exp_f32_e32 v48, v48
	v_exp_f32_e32 v49, v49
	v_exp_f32_e32 v52, v52
	v_exp_f32_e32 v53, v53
	v_pk_fma_f32 v[50:51], v[50:51], s[22:23], v[160:161] op_sel_hi:[1,0,1] neg_lo:[1,0,0] neg_hi:[1,0,0]
	v_pk_mul_f32 v[54:55], v[132:133], v[54:55]
	v_sqrt_f32_e32 v62, v62
	v_sqrt_f32_e32 v63, v63
	v_exp_f32_e32 v50, v50
	v_exp_f32_e32 v51, v51
	v_exp_f32_e32 v54, v54
	v_exp_f32_e32 v55, v55
	v_lshlrev_b32_e32 v66, 16, v141
	v_and_b32_e32 v67, 0xffff0000, v141
	v_pk_mul_f32 v[56:57], v[56:57], v[60:61]
	v_pk_mul_f32 v[58:59], v[58:59], v[66:67]
	v_pk_add_f32 v[48:49], v[48:49], 1.0 op_sel_hi:[1,0]
	v_pk_add_f32 v[60:61], v[52:53], 1.0 op_sel_hi:[1,0] neg_lo:[1,0] neg_hi:[1,0]
	v_pk_add_f32 v[52:53], v[52:53], 1.0 op_sel_hi:[1,0]
	v_pk_mul_f32 v[58:59], v[58:59], v[62:63]
	v_rcp_f32_e32 v48, v48
	v_rcp_f32_e32 v49, v49
	v_pk_mul_f32 v[52:53], v[60:61], v[52:53]
	v_pk_add_f32 v[50:51], v[50:51], 1.0 op_sel_hi:[1,0]
	v_pk_add_f32 v[62:63], v[54:55], 1.0 op_sel_hi:[1,0] neg_lo:[1,0] neg_hi:[1,0]
	v_pk_add_f32 v[54:55], v[54:55], 1.0 op_sel_hi:[1,0]
	v_sqrt_f32_e32 v52, v52
	v_sqrt_f32_e32 v53, v53
	v_rcp_f32_e32 v50, v50
	v_rcp_f32_e32 v51, v51
	v_pk_mul_f32 v[54:55], v[62:63], v[54:55]
	v_lshlrev_b32_e32 v68, 16, v142
	v_sqrt_f32_e32 v54, v54
	v_sqrt_f32_e32 v55, v55
	v_and_b32_e32 v69, 0xffff0000, v142
	v_lshlrev_b32_e32 v70, 16, v143
	v_and_b32_e32 v71, 0xffff0000, v143
	v_pk_mul_f32 v[48:49], v[48:49], v[68:69]
	s_nop 0
	v_pk_mul_f32 v[52:53], v[48:49], v[52:53]
	v_pk_mul_f32 v[48:49], v[50:51], v[70:71]
	v_cvt_pk_bf16_f32 v50, v60, v61
	v_add_co_u32_e32 v60, vcc, s74, v158
	v_pk_mul_f32 v[54:55], v[48:49], v[54:55]
	v_cvt_pk_bf16_f32 v48, v72, v73
	v_cvt_pk_bf16_f32 v49, v64, v65
	v_cvt_pk_bf16_f32 v51, v62, v63
	s_nop 0
	v_addc_co_u32_e32 v61, vcc, 0, v159, vcc
	global_store_dwordx4 v[60:61], v[48:51], off
	s_nop 1
	v_cvt_pk_bf16_f32 v48, v56, v57
	v_cvt_pk_bf16_f32 v49, v58, v59
	v_cvt_pk_bf16_f32 v50, v52, v53
	v_cvt_pk_bf16_f32 v51, v54, v55
	global_store_dwordx4 v[60:61], v[48:51], off offset:256
	v_pk_fma_f32 v[44:45], v[44:45], s[22:23], v[180:181] op_sel_hi:[1,0,1] neg_lo:[1,0,0] neg_hi:[1,0,0]
	v_pk_fma_f32 v[46:47], v[46:47], s[22:23], v[174:175] op_sel_hi:[1,0,1] neg_lo:[1,0,0] neg_hi:[1,0,0]
	v_exp_f32_e32 v44, v44
	v_exp_f32_e32 v45, v45
	v_exp_f32_e32 v46, v46
	v_exp_f32_e32 v47, v47
	v_pk_fma_f32 v[40:41], v[40:41], s[22:23], v[176:177] op_sel_hi:[1,0,1] neg_lo:[1,0,0] neg_hi:[1,0,0]
	v_pk_add_f32 v[44:45], v[44:45], 1.0 op_sel_hi:[1,0]
	v_pk_fma_f32 v[36:37], v[36:37], s[22:23], v[168:169] op_sel_hi:[1,0,1] neg_lo:[1,0,0] neg_hi:[1,0,0]
	v_rcp_f32_e32 v44, v44
	v_rcp_f32_e32 v45, v45
	v_pk_add_f32 v[46:47], v[46:47], 1.0 op_sel_hi:[1,0]
	v_exp_f32_e32 v40, v40
	v_exp_f32_e32 v41, v41
	v_rcp_f32_e32 v46, v46
	v_rcp_f32_e32 v47, v47
	v_exp_f32_e32 v36, v36
	v_exp_f32_e32 v37, v37
	v_pk_fma_f32 v[38:39], v[38:39], s[22:23], v[162:163] op_sel_hi:[1,0,1] neg_lo:[1,0,0] neg_hi:[1,0,0]
	v_pk_mul_f32 v[44:45], v[178:179], v[44:45]
	v_exp_f32_e32 v38, v38
	v_exp_f32_e32 v39, v39
	v_exp_f32_e32 v44, v44
	v_exp_f32_e32 v45, v45
	v_pk_add_f32 v[40:41], v[40:41], 1.0 op_sel_hi:[1,0]
	v_pk_fma_f32 v[42:43], v[42:43], s[22:23], v[170:171] op_sel_hi:[1,0,1] neg_lo:[1,0,0] neg_hi:[1,0,0]
	v_pk_mul_f32 v[46:47], v[172:173], v[46:47]
	v_pk_add_f32 v[36:37], v[36:37], 1.0 op_sel_hi:[1,0]
	v_rcp_f32_e32 v40, v40
	v_rcp_f32_e32 v41, v41
	v_exp_f32_e32 v42, v42
	v_exp_f32_e32 v43, v43
	v_exp_f32_e32 v46, v46
	v_exp_f32_e32 v47, v47
	v_rcp_f32_e32 v36, v36
	v_rcp_f32_e32 v37, v37
	v_pk_add_f32 v[38:39], v[38:39], 1.0 op_sel_hi:[1,0]
	s_waitcnt vmcnt(12)
	v_lshlrev_b32_e32 v48, 16, v136
	v_rcp_f32_e32 v38, v38
	v_rcp_f32_e32 v39, v39
	v_and_b32_e32 v49, 0xffff0000, v136
	v_pk_add_f32 v[56:57], v[44:45], 1.0 op_sel_hi:[1,0] neg_lo:[1,0] neg_hi:[1,0]
	v_pk_add_f32 v[44:45], v[44:45], 1.0 op_sel_hi:[1,0]
	v_pk_mul_f32 v[40:41], v[40:41], v[48:49]
	v_pk_mul_f32 v[44:45], v[56:57], v[44:45]
	v_pk_add_f32 v[42:43], v[42:43], 1.0 op_sel_hi:[1,0]
	v_pk_add_f32 v[48:49], v[46:47], 1.0 op_sel_hi:[1,0] neg_lo:[1,0] neg_hi:[1,0]
	v_pk_add_f32 v[46:47], v[46:47], 1.0 op_sel_hi:[1,0]
	v_pk_fma_f32 v[32:33], v[32:33], s[22:23], v[164:165] op_sel_hi:[1,0,1] neg_lo:[1,0,0] neg_hi:[1,0,0]
	v_pk_mul_f32 v[36:37], v[166:167], v[36:37]
	v_sqrt_f32_e32 v44, v44
	v_sqrt_f32_e32 v45, v45
	v_rcp_f32_e32 v42, v42
	v_rcp_f32_e32 v43, v43
	v_pk_mul_f32 v[46:47], v[48:49], v[46:47]
	v_exp_f32_e32 v32, v32
	v_exp_f32_e32 v33, v33
	v_exp_f32_e32 v36, v36
	v_exp_f32_e32 v37, v37
	v_pk_fma_f32 v[34:35], v[34:35], s[22:23], v[160:161] op_sel_hi:[1,0,1] neg_lo:[1,0,0] neg_hi:[1,0,0]
	v_pk_mul_f32 v[38:39], v[132:133], v[38:39]
	v_sqrt_f32_e32 v46, v46
	v_sqrt_f32_e32 v47, v47
	v_exp_f32_e32 v34, v34
	v_exp_f32_e32 v35, v35
	v_exp_f32_e32 v38, v38
	v_exp_f32_e32 v39, v39
	v_lshlrev_b32_e32 v50, 16, v137
	v_and_b32_e32 v51, 0xffff0000, v137
	v_pk_mul_f32 v[40:41], v[40:41], v[44:45]
	v_pk_mul_f32 v[42:43], v[42:43], v[50:51]
	v_pk_add_f32 v[32:33], v[32:33], 1.0 op_sel_hi:[1,0]
	v_pk_add_f32 v[44:45], v[36:37], 1.0 op_sel_hi:[1,0] neg_lo:[1,0] neg_hi:[1,0]
	v_pk_add_f32 v[36:37], v[36:37], 1.0 op_sel_hi:[1,0]
	v_pk_mul_f32 v[42:43], v[42:43], v[46:47]
	v_rcp_f32_e32 v32, v32
	v_rcp_f32_e32 v33, v33
	v_pk_mul_f32 v[36:37], v[44:45], v[36:37]
	v_pk_add_f32 v[34:35], v[34:35], 1.0 op_sel_hi:[1,0]
	v_pk_add_f32 v[46:47], v[38:39], 1.0 op_sel_hi:[1,0] neg_lo:[1,0] neg_hi:[1,0]
	v_pk_add_f32 v[38:39], v[38:39], 1.0 op_sel_hi:[1,0]
	v_sqrt_f32_e32 v36, v36
	v_sqrt_f32_e32 v37, v37
	v_rcp_f32_e32 v34, v34
	v_rcp_f32_e32 v35, v35
	v_pk_mul_f32 v[38:39], v[46:47], v[38:39]
	v_lshlrev_b32_e32 v52, 16, v138
	v_sqrt_f32_e32 v38, v38
	v_sqrt_f32_e32 v39, v39
	v_and_b32_e32 v53, 0xffff0000, v138
	v_lshlrev_b32_e32 v54, 16, v139
	v_and_b32_e32 v55, 0xffff0000, v139
	v_pk_mul_f32 v[32:33], v[32:33], v[52:53]
	s_nop 0
	v_pk_mul_f32 v[36:37], v[32:33], v[36:37]
	v_pk_mul_f32 v[32:33], v[34:35], v[54:55]
	v_cvt_pk_bf16_f32 v34, v44, v45
	v_add_co_u32_e32 v44, vcc, s75, v158
	v_pk_mul_f32 v[38:39], v[32:33], v[38:39]
	v_cvt_pk_bf16_f32 v32, v56, v57
	v_cvt_pk_bf16_f32 v33, v48, v49
	v_cvt_pk_bf16_f32 v35, v46, v47
	s_nop 0
	v_addc_co_u32_e32 v45, vcc, 0, v159, vcc
	global_store_dwordx4 v[44:45], v[32:35], off
	s_nop 1
	v_cvt_pk_bf16_f32 v32, v40, v41
	v_cvt_pk_bf16_f32 v33, v42, v43
	v_cvt_pk_bf16_f32 v34, v36, v37
	v_cvt_pk_bf16_f32 v35, v38, v39
	global_store_dwordx4 v[44:45], v[32:35], off offset:256
	v_pk_fma_f32 v[28:29], v[28:29], s[22:23], v[180:181] op_sel_hi:[1,0,1] neg_lo:[1,0,0] neg_hi:[1,0,0]
	v_pk_fma_f32 v[30:31], v[30:31], s[22:23], v[174:175] op_sel_hi:[1,0,1] neg_lo:[1,0,0] neg_hi:[1,0,0]
	v_exp_f32_e32 v28, v28
	v_exp_f32_e32 v29, v29
	v_exp_f32_e32 v30, v30
	v_exp_f32_e32 v31, v31
	v_pk_fma_f32 v[24:25], v[24:25], s[22:23], v[176:177] op_sel_hi:[1,0,1] neg_lo:[1,0,0] neg_hi:[1,0,0]
	v_pk_add_f32 v[28:29], v[28:29], 1.0 op_sel_hi:[1,0]
	v_pk_fma_f32 v[20:21], v[20:21], s[22:23], v[168:169] op_sel_hi:[1,0,1] neg_lo:[1,0,0] neg_hi:[1,0,0]
	v_rcp_f32_e32 v28, v28
	v_rcp_f32_e32 v29, v29
	v_pk_add_f32 v[30:31], v[30:31], 1.0 op_sel_hi:[1,0]
	v_exp_f32_e32 v24, v24
	v_exp_f32_e32 v25, v25
	v_rcp_f32_e32 v30, v30
	v_rcp_f32_e32 v31, v31
	v_exp_f32_e32 v20, v20
	v_exp_f32_e32 v21, v21
	v_pk_fma_f32 v[22:23], v[22:23], s[22:23], v[162:163] op_sel_hi:[1,0,1] neg_lo:[1,0,0] neg_hi:[1,0,0]
	v_pk_mul_f32 v[28:29], v[178:179], v[28:29]
	v_exp_f32_e32 v22, v22
	v_exp_f32_e32 v23, v23
	v_exp_f32_e32 v28, v28
	v_exp_f32_e32 v29, v29
	v_pk_add_f32 v[24:25], v[24:25], 1.0 op_sel_hi:[1,0]
	v_pk_fma_f32 v[26:27], v[26:27], s[22:23], v[170:171] op_sel_hi:[1,0,1] neg_lo:[1,0,0] neg_hi:[1,0,0]
	v_pk_mul_f32 v[30:31], v[172:173], v[30:31]
	v_pk_add_f32 v[20:21], v[20:21], 1.0 op_sel_hi:[1,0]
	v_rcp_f32_e32 v24, v24
	v_rcp_f32_e32 v25, v25
	v_exp_f32_e32 v26, v26
	v_exp_f32_e32 v27, v27
	v_exp_f32_e32 v30, v30
	v_exp_f32_e32 v31, v31
	v_rcp_f32_e32 v20, v20
	v_rcp_f32_e32 v21, v21
	v_pk_add_f32 v[22:23], v[22:23], 1.0 op_sel_hi:[1,0]
	s_waitcnt vmcnt(13)
	v_lshlrev_b32_e32 v32, 16, v116
	v_rcp_f32_e32 v22, v22
	v_rcp_f32_e32 v23, v23
	v_and_b32_e32 v33, 0xffff0000, v116
	v_pk_add_f32 v[40:41], v[28:29], 1.0 op_sel_hi:[1,0] neg_lo:[1,0] neg_hi:[1,0]
	v_pk_add_f32 v[28:29], v[28:29], 1.0 op_sel_hi:[1,0]
	v_pk_mul_f32 v[24:25], v[24:25], v[32:33]
	v_pk_mul_f32 v[28:29], v[40:41], v[28:29]
	v_pk_add_f32 v[26:27], v[26:27], 1.0 op_sel_hi:[1,0]
	v_pk_add_f32 v[32:33], v[30:31], 1.0 op_sel_hi:[1,0] neg_lo:[1,0] neg_hi:[1,0]
	v_pk_add_f32 v[30:31], v[30:31], 1.0 op_sel_hi:[1,0]
	v_pk_fma_f32 v[16:17], v[16:17], s[22:23], v[164:165] op_sel_hi:[1,0,1] neg_lo:[1,0,0] neg_hi:[1,0,0]
	v_pk_mul_f32 v[20:21], v[166:167], v[20:21]
	v_sqrt_f32_e32 v28, v28
	v_sqrt_f32_e32 v29, v29
	v_rcp_f32_e32 v26, v26
	v_rcp_f32_e32 v27, v27
	v_pk_mul_f32 v[30:31], v[32:33], v[30:31]
	v_exp_f32_e32 v16, v16
	v_exp_f32_e32 v17, v17
	v_exp_f32_e32 v20, v20
	v_exp_f32_e32 v21, v21
	v_pk_fma_f32 v[18:19], v[18:19], s[22:23], v[160:161] op_sel_hi:[1,0,1] neg_lo:[1,0,0] neg_hi:[1,0,0]
	v_pk_mul_f32 v[22:23], v[132:133], v[22:23]
	v_sqrt_f32_e32 v30, v30
	v_sqrt_f32_e32 v31, v31
	v_exp_f32_e32 v18, v18
	v_exp_f32_e32 v19, v19
	v_exp_f32_e32 v22, v22
	v_exp_f32_e32 v23, v23
	v_lshlrev_b32_e32 v34, 16, v117
	v_and_b32_e32 v35, 0xffff0000, v117
	v_pk_mul_f32 v[24:25], v[24:25], v[28:29]
	v_pk_mul_f32 v[26:27], v[26:27], v[34:35]
	v_pk_add_f32 v[16:17], v[16:17], 1.0 op_sel_hi:[1,0]
	v_pk_add_f32 v[28:29], v[20:21], 1.0 op_sel_hi:[1,0] neg_lo:[1,0] neg_hi:[1,0]
	v_pk_add_f32 v[20:21], v[20:21], 1.0 op_sel_hi:[1,0]
	v_pk_mul_f32 v[26:27], v[26:27], v[30:31]
	v_rcp_f32_e32 v16, v16
	v_rcp_f32_e32 v17, v17
	v_pk_mul_f32 v[20:21], v[28:29], v[20:21]
	v_pk_add_f32 v[18:19], v[18:19], 1.0 op_sel_hi:[1,0]
	v_pk_add_f32 v[30:31], v[22:23], 1.0 op_sel_hi:[1,0] neg_lo:[1,0] neg_hi:[1,0]
	v_pk_add_f32 v[22:23], v[22:23], 1.0 op_sel_hi:[1,0]
	v_sqrt_f32_e32 v20, v20
	v_sqrt_f32_e32 v21, v21
	v_rcp_f32_e32 v18, v18
	v_rcp_f32_e32 v19, v19
	v_pk_mul_f32 v[22:23], v[30:31], v[22:23]
	v_lshlrev_b32_e32 v36, 16, v118
	v_sqrt_f32_e32 v22, v22
	v_sqrt_f32_e32 v23, v23
	v_and_b32_e32 v37, 0xffff0000, v118
	v_lshlrev_b32_e32 v38, 16, v119
	v_and_b32_e32 v39, 0xffff0000, v119
	v_pk_mul_f32 v[16:17], v[16:17], v[36:37]
	s_nop 0
	v_pk_mul_f32 v[20:21], v[16:17], v[20:21]
	v_pk_mul_f32 v[16:17], v[18:19], v[38:39]
	v_cvt_pk_bf16_f32 v18, v28, v29
	v_add_co_u32_e32 v28, vcc, s76, v158
	v_pk_mul_f32 v[22:23], v[16:17], v[22:23]
	v_cvt_pk_bf16_f32 v16, v40, v41
	v_cvt_pk_bf16_f32 v17, v32, v33
	v_cvt_pk_bf16_f32 v19, v30, v31
	s_nop 0
	v_addc_co_u32_e32 v29, vcc, 0, v159, vcc
	global_store_dwordx4 v[28:29], v[16:19], off
	s_nop 1
	v_cvt_pk_bf16_f32 v16, v24, v25
	v_cvt_pk_bf16_f32 v17, v26, v27
	v_cvt_pk_bf16_f32 v18, v20, v21
	v_cvt_pk_bf16_f32 v19, v22, v23
	global_store_dwordx4 v[28:29], v[16:19], off offset:256
	v_pk_fma_f32 v[12:13], v[12:13], s[22:23], v[180:181] op_sel_hi:[1,0,1] neg_lo:[1,0,0] neg_hi:[1,0,0]
	v_pk_fma_f32 v[14:15], v[14:15], s[22:23], v[174:175] op_sel_hi:[1,0,1] neg_lo:[1,0,0] neg_hi:[1,0,0]
	v_exp_f32_e32 v12, v12
	v_exp_f32_e32 v13, v13
	v_exp_f32_e32 v14, v14
	v_exp_f32_e32 v15, v15
	v_pk_fma_f32 v[8:9], v[8:9], s[22:23], v[176:177] op_sel_hi:[1,0,1] neg_lo:[1,0,0] neg_hi:[1,0,0]
	v_pk_add_f32 v[12:13], v[12:13], 1.0 op_sel_hi:[1,0]
	v_pk_fma_f32 v[4:5], v[4:5], s[22:23], v[168:169] op_sel_hi:[1,0,1] neg_lo:[1,0,0] neg_hi:[1,0,0]
	v_rcp_f32_e32 v12, v12
	v_rcp_f32_e32 v13, v13
	v_pk_add_f32 v[14:15], v[14:15], 1.0 op_sel_hi:[1,0]
	v_exp_f32_e32 v8, v8
	v_exp_f32_e32 v9, v9
	v_rcp_f32_e32 v14, v14
	v_rcp_f32_e32 v15, v15
	v_exp_f32_e32 v4, v4
	v_exp_f32_e32 v5, v5
	v_pk_fma_f32 v[6:7], v[6:7], s[22:23], v[162:163] op_sel_hi:[1,0,1] neg_lo:[1,0,0] neg_hi:[1,0,0]
	v_pk_mul_f32 v[12:13], v[178:179], v[12:13]
	v_exp_f32_e32 v6, v6
	v_exp_f32_e32 v7, v7
	v_exp_f32_e32 v12, v12
	v_exp_f32_e32 v13, v13
	v_pk_add_f32 v[8:9], v[8:9], 1.0 op_sel_hi:[1,0]
	v_pk_fma_f32 v[10:11], v[10:11], s[22:23], v[170:171] op_sel_hi:[1,0,1] neg_lo:[1,0,0] neg_hi:[1,0,0]
	v_pk_mul_f32 v[14:15], v[172:173], v[14:15]
	v_pk_add_f32 v[4:5], v[4:5], 1.0 op_sel_hi:[1,0]
	v_rcp_f32_e32 v8, v8
	v_rcp_f32_e32 v9, v9
	v_exp_f32_e32 v10, v10
	v_exp_f32_e32 v11, v11
	v_exp_f32_e32 v14, v14
	v_exp_f32_e32 v15, v15
	v_rcp_f32_e32 v4, v4
	v_rcp_f32_e32 v5, v5
	v_pk_add_f32 v[6:7], v[6:7], 1.0 op_sel_hi:[1,0]
	s_waitcnt vmcnt(14)
	v_lshlrev_b32_e32 v16, 16, v96
	v_rcp_f32_e32 v6, v6
	v_rcp_f32_e32 v7, v7
	v_and_b32_e32 v17, 0xffff0000, v96
	v_pk_add_f32 v[24:25], v[12:13], 1.0 op_sel_hi:[1,0] neg_lo:[1,0] neg_hi:[1,0]
	v_pk_add_f32 v[12:13], v[12:13], 1.0 op_sel_hi:[1,0]
	v_pk_mul_f32 v[8:9], v[8:9], v[16:17]
	v_pk_mul_f32 v[12:13], v[24:25], v[12:13]
	v_pk_add_f32 v[10:11], v[10:11], 1.0 op_sel_hi:[1,0]
	v_pk_add_f32 v[16:17], v[14:15], 1.0 op_sel_hi:[1,0] neg_lo:[1,0] neg_hi:[1,0]
	v_pk_add_f32 v[14:15], v[14:15], 1.0 op_sel_hi:[1,0]
	v_pk_fma_f32 v[0:1], v[0:1], s[22:23], v[164:165] op_sel_hi:[1,0,1] neg_lo:[1,0,0] neg_hi:[1,0,0]
	v_pk_mul_f32 v[4:5], v[166:167], v[4:5]
	v_sqrt_f32_e32 v12, v12
	v_sqrt_f32_e32 v13, v13
	v_rcp_f32_e32 v10, v10
	v_rcp_f32_e32 v11, v11
	v_pk_mul_f32 v[14:15], v[16:17], v[14:15]
	v_exp_f32_e32 v0, v0
	v_exp_f32_e32 v1, v1
	v_exp_f32_e32 v4, v4
	v_exp_f32_e32 v5, v5
	v_pk_fma_f32 v[2:3], v[2:3], s[22:23], v[160:161] op_sel_hi:[1,0,1] neg_lo:[1,0,0] neg_hi:[1,0,0]
	v_pk_mul_f32 v[6:7], v[132:133], v[6:7]
	v_sqrt_f32_e32 v14, v14
	v_sqrt_f32_e32 v15, v15
	v_exp_f32_e32 v2, v2
	v_exp_f32_e32 v3, v3
	v_exp_f32_e32 v6, v6
	v_exp_f32_e32 v7, v7
	v_lshlrev_b32_e32 v18, 16, v97
	v_and_b32_e32 v19, 0xffff0000, v97
	v_pk_mul_f32 v[8:9], v[8:9], v[12:13]
	v_pk_mul_f32 v[10:11], v[10:11], v[18:19]
	v_pk_add_f32 v[0:1], v[0:1], 1.0 op_sel_hi:[1,0]
	v_pk_add_f32 v[12:13], v[4:5], 1.0 op_sel_hi:[1,0] neg_lo:[1,0] neg_hi:[1,0]
	v_pk_add_f32 v[4:5], v[4:5], 1.0 op_sel_hi:[1,0]
	v_pk_mul_f32 v[10:11], v[10:11], v[14:15]
	v_rcp_f32_e32 v0, v0
	v_rcp_f32_e32 v1, v1
	v_pk_mul_f32 v[4:5], v[12:13], v[4:5]
	v_pk_add_f32 v[2:3], v[2:3], 1.0 op_sel_hi:[1,0]
	v_pk_add_f32 v[14:15], v[6:7], 1.0 op_sel_hi:[1,0] neg_lo:[1,0] neg_hi:[1,0]
	v_pk_add_f32 v[6:7], v[6:7], 1.0 op_sel_hi:[1,0]
	v_sqrt_f32_e32 v4, v4
	v_sqrt_f32_e32 v5, v5
	v_rcp_f32_e32 v2, v2
	v_rcp_f32_e32 v3, v3
	v_pk_mul_f32 v[6:7], v[14:15], v[6:7]
	v_lshlrev_b32_e32 v20, 16, v98
	v_sqrt_f32_e32 v6, v6
	v_sqrt_f32_e32 v7, v7
	v_and_b32_e32 v21, 0xffff0000, v98
	v_lshlrev_b32_e32 v22, 16, v99
	v_and_b32_e32 v23, 0xffff0000, v99
	v_pk_mul_f32 v[0:1], v[0:1], v[20:21]
	s_nop 0
	v_pk_mul_f32 v[4:5], v[0:1], v[4:5]
	v_pk_mul_f32 v[0:1], v[2:3], v[22:23]
	v_cvt_pk_bf16_f32 v2, v12, v13
	v_add_co_u32_e32 v12, vcc, 0x160000, v158
	v_pk_mul_f32 v[6:7], v[0:1], v[6:7]
	v_cvt_pk_bf16_f32 v0, v24, v25
	v_cvt_pk_bf16_f32 v1, v16, v17
	v_cvt_pk_bf16_f32 v3, v14, v15
	s_nop 0
	v_addc_co_u32_e32 v13, vcc, 0, v159, vcc
	global_store_dwordx4 v[12:13], v[0:3], off
	s_nop 1
	v_cvt_pk_bf16_f32 v0, v8, v9
	v_cvt_pk_bf16_f32 v1, v10, v11
	v_cvt_pk_bf16_f32 v2, v4, v5
	v_cvt_pk_bf16_f32 v3, v6, v7
	global_store_dwordx4 v[12:13], v[0:3], off offset:256
	s_and_b64 vcc, exec, s[6:7]
	s_mov_b64 s[6:7], -1
	s_cbranch_vccnz .LBB0_1268
	s_andn2_b64 vcc, exec, s[14:15]
	s_cbranch_vccnz .LBB0_1267
	s_barrier
	s_branch .LBB0_1267
